# P2: sink s_load issued at the sub-block head, its lgkmcnt wait and scaling deferred to just before the key loop
# baseline (speedup 1.0000x reference)
.LBB0_306:
	s_mul_i32 s12, s22, s55
	s_sub_i32 s14, s7, s12
	s_and_b64 s[12:13], s[86:87], exec
	s_cselect_b32 s50, s14, 0
	s_andn2_b64 vcc, exec, s[0:1]
	s_cbranch_vccnz .LBB0_308
	s_ashr_i32 s51, s50, 31
	s_lshl_b64 s[12:13], s[50:51], 2
	s_add_u32 s12, s44, s12
	s_addc_u32 s13, s45, s13
	s_load_dword s99, s[12:13], 0x0
	s_mov_b32 s98, 1
	s_mov_b32 s12, 1.0
	s_branch .LBB0_309
.LBB0_308:
	s_mov_b32 s12, 0
	s_mov_b32 s98, 0
	v_mov_b32_e32 v205, 0xf149f2ca

.LBB0_323:
	s_cmp_eq_u32 s98, 0
	s_cbranch_scc1 .Lsink_done
	s_waitcnt lgkmcnt(0)
	v_mov_b32_e32 v3, s99
	v_mul_f32_e32 v205, 0x3fb8aa3b, v3
